# FoX attention epilogue: the four gate loads of each output row issued together at the top of the row (one wait per row) instead of load, wait, multiply, store per element; placement kept
# speedup vs baseline: 1.0105x; 1.0071x over previous
; __device__ __forceinline__ unsigned cvt_pk_bf16(float lo, float hi) { unsigned r; asm volatile("v_cvt_pk_bf16_f32 %0, %1, %2" : "=v"(r) : "v"(lo), "v"(hi)); return r; }
; __device__ __forceinline__ float bf_lo(unsigned w) { return __uint_as_float(w << 16); }
; __device__ __forceinline__ float bf_hi(unsigned w) { return __uint_as_float(w & 0xffff0000u); }
; __device__ __forceinline__ int crow(int r, int hi) { return (r & 3) + 8 * (r >> 2) + 4 * hi; }
; template <int MODE> ...
;     ...
;     if (hi == 0) li_l[r32] = l_reg; asm volatile("s_waitcnt lgkmcnt(0)" ::: "memory");
; #pragma unroll
;     for (int r = 0; r < 16; ++r) { const int orow = qlo + crow(r, hi); const float rl = __builtin_amdgcn_rcpf(li_l[crow(r, hi)]);
; #pragma unroll
;         for (int d0 = 0; d0 < 4; ++d0) { float v = o[d0][r] * rl; float vn = __shfl_xor(v, 1);
;             if ((r32 & 1) == 0) { const int col = d0 * 32 + r32;
;                 if (MODE == 1) { const unsigned g = *(const unsigned*)(gate + (size_t)orow * 1024 + hoff + col); v *= bf_lo(g); vn *= bf_hi(g); }
;                 *(unsigned*)(Ob + (size_t)orow * DM + ocol0 + col) = cvt_pk_bf16(v, vn); } } }
.LBB0_1420:
	s_or_b64 exec, exec, s[0:1]
	ds_read_b32 v5, v160 offset:4
	v_add3_u32 v6, s10, v162, 1
	v_ashrrev_i32_e32 v7, 31, v6
	v_lshlrev_b64 v[8:9], 11, v[6:7]
	v_lshlrev_b64 v[6:7], 12, v[6:7]
	s_waitcnt lgkmcnt(0)
	v_rcp_f32_e32 v5, v5
	v_lshl_add_u64 v[8:9], s[6:7], 0, v[8:9]
	v_lshl_add_u64 v[6:7], s[8:9], 0, v[6:7]
	v_lshl_add_u64 v[242:243], v[8:9], 0, v[2:3]
	global_load_dword v244, v[242:243], off
	global_load_dword v245, v[242:243], off offset:64
	global_load_dword v246, v[242:243], off offset:128
	global_load_dword v247, v[242:243], off offset:192
	v_mul_f32_e32 v11, v67, v5
	ds_bpermute_b32 v12, v10, v11
	s_and_saveexec_b64 s[0:1], s[2:3]
	s_cbranch_execz .LBB0_1422
	v_lshl_add_u64 v[14:15], v[8:9], 0, v[2:3]
	s_waitcnt vmcnt(0)
	v_mov_b32_e32 v13, v244
	v_lshlrev_b32_e32 v14, 16, v13
	v_and_b32_e32 v13, 0xffff0000, v13
	v_mul_f32_e32 v11, v11, v14
	s_waitcnt lgkmcnt(0)
	v_mul_f32_e32 v12, v12, v13
	v_cvt_pk_bf16_f32 v11, v11, v12
	v_lshl_add_u64 v[12:13], v[6:7], 0, v[2:3]
	global_store_dword v[12:13], v11, off
.LBB0_1422:
	s_or_b64 exec, exec, s[0:1]
	v_mul_f32_e32 v11, v51, v5
	s_waitcnt lgkmcnt(0)
	ds_bpermute_b32 v12, v10, v11
	s_and_saveexec_b64 s[0:1], s[2:3]
	s_cbranch_execz .LBB0_1424
	v_lshl_add_u64 v[14:15], v[8:9], 0, v[2:3]
	v_mov_b32_e32 v13, v245
	v_lshlrev_b32_e32 v14, 16, v13
	v_and_b32_e32 v13, 0xffff0000, v13
	v_mul_f32_e32 v11, v11, v14
	s_waitcnt lgkmcnt(0)
	v_mul_f32_e32 v12, v12, v13
	v_cvt_pk_bf16_f32 v11, v11, v12
	v_lshl_add_u64 v[12:13], v[6:7], 0, v[2:3]
	global_store_dword v[12:13], v11, off offset:64
.LBB0_1424:
	s_or_b64 exec, exec, s[0:1]
	v_mul_f32_e32 v11, v35, v5
	s_waitcnt lgkmcnt(0)
	ds_bpermute_b32 v12, v10, v11
	s_and_saveexec_b64 s[0:1], s[2:3]
	s_cbranch_execz .LBB0_1426
	v_lshl_add_u64 v[14:15], v[8:9], 0, v[2:3]
	v_mov_b32_e32 v13, v246
	v_lshlrev_b32_e32 v14, 16, v13
	v_and_b32_e32 v13, 0xffff0000, v13
	v_mul_f32_e32 v11, v11, v14
	s_waitcnt lgkmcnt(0)
	v_mul_f32_e32 v12, v12, v13
	v_cvt_pk_bf16_f32 v11, v11, v12
	v_lshl_add_u64 v[12:13], v[6:7], 0, v[2:3]
	global_store_dword v[12:13], v11, off offset:128
.LBB0_1426:
	s_or_b64 exec, exec, s[0:1]
	v_mul_f32_e32 v5, v19, v5
	ds_bpermute_b32 v11, v10, v5
	s_and_saveexec_b64 s[0:1], s[2:3]
	s_cbranch_execz .LBB0_1428
	v_lshl_add_u64 v[8:9], v[8:9], 0, v[2:3]
	v_lshl_add_u64 v[6:7], v[6:7], 0, v[2:3]
	v_mov_b32_e32 v8, v247
	v_lshlrev_b32_e32 v9, 16, v8
	v_and_b32_e32 v8, 0xffff0000, v8
	v_mul_f32_e32 v5, v5, v9
	s_waitcnt lgkmcnt(0)
	v_mul_f32_e32 v8, v11, v8
	v_cvt_pk_bf16_f32 v5, v5, v8
	global_store_dword v[6:7], v5, off offset:192
.LBB0_1428:
	s_or_b64 exec, exec, s[0:1]
	ds_read_b32 v5, v160 offset:8
	v_add3_u32 v6, s10, v162, 2
	v_ashrrev_i32_e32 v7, 31, v6
	v_lshlrev_b64 v[8:9], 11, v[6:7]
	v_lshlrev_b64 v[6:7], 12, v[6:7]
	s_waitcnt lgkmcnt(0)
	v_rcp_f32_e32 v5, v5
	v_lshl_add_u64 v[8:9], s[6:7], 0, v[8:9]
	v_lshl_add_u64 v[6:7], s[8:9], 0, v[6:7]
	v_lshl_add_u64 v[242:243], v[8:9], 0, v[2:3]
	global_load_dword v244, v[242:243], off
	global_load_dword v245, v[242:243], off offset:64
	global_load_dword v246, v[242:243], off offset:128
	global_load_dword v247, v[242:243], off offset:192
	v_mul_f32_e32 v11, v68, v5
	ds_bpermute_b32 v12, v10, v11
	s_and_saveexec_b64 s[0:1], s[2:3]
	s_cbranch_execz .LBB0_1430
	v_lshl_add_u64 v[14:15], v[8:9], 0, v[2:3]
	s_waitcnt vmcnt(0)
	v_mov_b32_e32 v13, v244
	v_lshlrev_b32_e32 v14, 16, v13
	v_and_b32_e32 v13, 0xffff0000, v13
	v_mul_f32_e32 v11, v11, v14
	s_waitcnt lgkmcnt(0)
	v_mul_f32_e32 v12, v12, v13
	v_cvt_pk_bf16_f32 v11, v11, v12
	v_lshl_add_u64 v[12:13], v[6:7], 0, v[2:3]
	global_store_dword v[12:13], v11, off
.LBB0_1430:
	s_or_b64 exec, exec, s[0:1]
	v_mul_f32_e32 v11, v52, v5
	s_waitcnt lgkmcnt(0)
	ds_bpermute_b32 v12, v10, v11
	s_and_saveexec_b64 s[0:1], s[2:3]
	s_cbranch_execz .LBB0_1432
	v_lshl_add_u64 v[14:15], v[8:9], 0, v[2:3]
	v_mov_b32_e32 v13, v245
	v_lshlrev_b32_e32 v14, 16, v13
	v_and_b32_e32 v13, 0xffff0000, v13
	v_mul_f32_e32 v11, v11, v14
	s_waitcnt lgkmcnt(0)
	v_mul_f32_e32 v12, v12, v13
	v_cvt_pk_bf16_f32 v11, v11, v12
	v_lshl_add_u64 v[12:13], v[6:7], 0, v[2:3]
	global_store_dword v[12:13], v11, off offset:64
.LBB0_1432:
	s_or_b64 exec, exec, s[0:1]
	v_mul_f32_e32 v11, v36, v5
	s_waitcnt lgkmcnt(0)
	ds_bpermute_b32 v12, v10, v11
	s_and_saveexec_b64 s[0:1], s[2:3]
	s_cbranch_execz .LBB0_1434
	v_lshl_add_u64 v[14:15], v[8:9], 0, v[2:3]
	v_mov_b32_e32 v13, v246
	v_lshlrev_b32_e32 v14, 16, v13
	v_and_b32_e32 v13, 0xffff0000, v13
	v_mul_f32_e32 v11, v11, v14
	s_waitcnt lgkmcnt(0)
	v_mul_f32_e32 v12, v12, v13
	v_cvt_pk_bf16_f32 v11, v11, v12
	v_lshl_add_u64 v[12:13], v[6:7], 0, v[2:3]
	global_store_dword v[12:13], v11, off offset:128
.LBB0_1434:
	s_or_b64 exec, exec, s[0:1]
	v_mul_f32_e32 v5, v20, v5
	ds_bpermute_b32 v11, v10, v5
	s_and_saveexec_b64 s[0:1], s[2:3]
	s_cbranch_execz .LBB0_1436
	v_lshl_add_u64 v[8:9], v[8:9], 0, v[2:3]
	v_lshl_add_u64 v[6:7], v[6:7], 0, v[2:3]
	v_mov_b32_e32 v8, v247
	v_lshlrev_b32_e32 v9, 16, v8
	v_and_b32_e32 v8, 0xffff0000, v8
	v_mul_f32_e32 v5, v5, v9
	s_waitcnt lgkmcnt(0)
	v_mul_f32_e32 v8, v11, v8
	v_cvt_pk_bf16_f32 v5, v5, v8
	global_store_dword v[6:7], v5, off offset:192
; __device__ __forceinline__ unsigned cvt_pk_bf16(float lo, float hi) { unsigned r; asm volatile("v_cvt_pk_bf16_f32 %0, %1, %2" : "=v"(r) : "v"(lo), "v"(hi)); return r; }
; __device__ __forceinline__ float bf_lo(unsigned w) { return __uint_as_float(w << 16); }
; __device__ __forceinline__ float bf_hi(unsigned w) { return __uint_as_float(w & 0xffff0000u); }
; __device__ __forceinline__ int crow(int r, int hi) { return (r & 3) + 8 * (r >> 2) + 4 * hi; }
; template <int MODE> ...
;     ...
;     if (hi == 0) li_l[r32] = l_reg; asm volatile("s_waitcnt lgkmcnt(0)" ::: "memory");
; #pragma unroll
;     for (int r = 0; r < 16; ++r) { const int orow = qlo + crow(r, hi); const float rl = __builtin_amdgcn_rcpf(li_l[crow(r, hi)]);
; #pragma unroll
;         for (int d0 = 0; d0 < 4; ++d0) { float v = o[d0][r] * rl; float vn = __shfl_xor(v, 1);
;             if ((r32 & 1) == 0) { const int col = d0 * 32 + r32;
;                 if (MODE == 1) { const unsigned g = *(const unsigned*)(gate + (size_t)orow * 1024 + hoff + col); v *= bf_lo(g); vn *= bf_hi(g); }
;                 *(unsigned*)(Ob + (size_t)orow * DM + ocol0 + col) = cvt_pk_bf16(v, vn); } } }
.LBB0_1436:
	s_or_b64 exec, exec, s[0:1]
	ds_read_b32 v5, v160 offset:12
	v_add3_u32 v6, s10, v162, 3
	v_ashrrev_i32_e32 v7, 31, v6
	v_lshlrev_b64 v[8:9], 11, v[6:7]
	v_lshlrev_b64 v[6:7], 12, v[6:7]
	s_waitcnt lgkmcnt(0)
	v_rcp_f32_e32 v5, v5
	v_lshl_add_u64 v[8:9], s[6:7], 0, v[8:9]
	v_lshl_add_u64 v[6:7], s[8:9], 0, v[6:7]
	v_lshl_add_u64 v[242:243], v[8:9], 0, v[2:3]
	global_load_dword v244, v[242:243], off
	global_load_dword v245, v[242:243], off offset:64
	global_load_dword v246, v[242:243], off offset:128
	global_load_dword v247, v[242:243], off offset:192
	v_mul_f32_e32 v11, v69, v5
	ds_bpermute_b32 v12, v10, v11
	s_and_saveexec_b64 s[0:1], s[2:3]
	s_cbranch_execz .LBB0_1438
	v_lshl_add_u64 v[14:15], v[8:9], 0, v[2:3]
	s_waitcnt vmcnt(0)
	v_mov_b32_e32 v13, v244
	v_lshlrev_b32_e32 v14, 16, v13
	v_and_b32_e32 v13, 0xffff0000, v13
	v_mul_f32_e32 v11, v11, v14
	s_waitcnt lgkmcnt(0)
	v_mul_f32_e32 v12, v12, v13
	v_cvt_pk_bf16_f32 v11, v11, v12
	v_lshl_add_u64 v[12:13], v[6:7], 0, v[2:3]
	global_store_dword v[12:13], v11, off
.LBB0_1438:
	s_or_b64 exec, exec, s[0:1]
	v_mul_f32_e32 v11, v53, v5
	s_waitcnt lgkmcnt(0)
	ds_bpermute_b32 v12, v10, v11
	s_and_saveexec_b64 s[0:1], s[2:3]
	s_cbranch_execz .LBB0_1440
	v_lshl_add_u64 v[14:15], v[8:9], 0, v[2:3]
	v_mov_b32_e32 v13, v245
	v_lshlrev_b32_e32 v14, 16, v13
	v_and_b32_e32 v13, 0xffff0000, v13
	v_mul_f32_e32 v11, v11, v14
	s_waitcnt lgkmcnt(0)
	v_mul_f32_e32 v12, v12, v13
	v_cvt_pk_bf16_f32 v11, v11, v12
	v_lshl_add_u64 v[12:13], v[6:7], 0, v[2:3]
	global_store_dword v[12:13], v11, off offset:64
.LBB0_1440:
	s_or_b64 exec, exec, s[0:1]
	v_mul_f32_e32 v11, v37, v5
	s_waitcnt lgkmcnt(0)
	ds_bpermute_b32 v12, v10, v11
	s_and_saveexec_b64 s[0:1], s[2:3]
	s_cbranch_execz .LBB0_1442
	v_lshl_add_u64 v[14:15], v[8:9], 0, v[2:3]
	v_mov_b32_e32 v13, v246
	v_lshlrev_b32_e32 v14, 16, v13
	v_and_b32_e32 v13, 0xffff0000, v13
	v_mul_f32_e32 v11, v11, v14
	s_waitcnt lgkmcnt(0)
	v_mul_f32_e32 v12, v12, v13
	v_cvt_pk_bf16_f32 v11, v11, v12
	v_lshl_add_u64 v[12:13], v[6:7], 0, v[2:3]
	global_store_dword v[12:13], v11, off offset:128
.LBB0_1442:
	s_or_b64 exec, exec, s[0:1]
	v_mul_f32_e32 v5, v21, v5
	ds_bpermute_b32 v11, v10, v5
	s_and_saveexec_b64 s[0:1], s[2:3]
	s_cbranch_execz .LBB0_1444
	v_lshl_add_u64 v[8:9], v[8:9], 0, v[2:3]
	v_lshl_add_u64 v[6:7], v[6:7], 0, v[2:3]
	v_mov_b32_e32 v8, v247
	v_lshlrev_b32_e32 v9, 16, v8
	v_and_b32_e32 v8, 0xffff0000, v8
	v_mul_f32_e32 v5, v5, v9
	s_waitcnt lgkmcnt(0)
	v_mul_f32_e32 v8, v11, v8
	v_cvt_pk_bf16_f32 v5, v5, v8
	global_store_dword v[6:7], v5, off offset:192
.LBB0_1444:
	s_or_b64 exec, exec, s[0:1]
	ds_read_b32 v5, v160 offset:32
	v_add_u32_e32 v6, 8, v4
	v_ashrrev_i32_e32 v7, 31, v6
	v_lshlrev_b64 v[8:9], 11, v[6:7]
	v_lshlrev_b64 v[6:7], 12, v[6:7]
	s_waitcnt lgkmcnt(0)
	v_rcp_f32_e32 v5, v5
	v_lshl_add_u64 v[8:9], s[6:7], 0, v[8:9]
	v_lshl_add_u64 v[6:7], s[8:9], 0, v[6:7]
	v_lshl_add_u64 v[242:243], v[8:9], 0, v[2:3]
	global_load_dword v244, v[242:243], off
	global_load_dword v245, v[242:243], off offset:64
	global_load_dword v246, v[242:243], off offset:128
	global_load_dword v247, v[242:243], off offset:192
	v_mul_f32_e32 v11, v70, v5
	ds_bpermute_b32 v12, v10, v11
	s_and_saveexec_b64 s[0:1], s[2:3]
	s_cbranch_execz .LBB0_1446
	v_lshl_add_u64 v[14:15], v[8:9], 0, v[2:3]
	s_waitcnt vmcnt(0)
	v_mov_b32_e32 v13, v244
	v_lshlrev_b32_e32 v14, 16, v13
	v_and_b32_e32 v13, 0xffff0000, v13
	v_mul_f32_e32 v11, v11, v14
	s_waitcnt lgkmcnt(0)
	v_mul_f32_e32 v12, v12, v13
	v_cvt_pk_bf16_f32 v11, v11, v12
	v_lshl_add_u64 v[12:13], v[6:7], 0, v[2:3]
	global_store_dword v[12:13], v11, off
.LBB0_1446:
	s_or_b64 exec, exec, s[0:1]
	v_mul_f32_e32 v11, v54, v5
	s_waitcnt lgkmcnt(0)
	ds_bpermute_b32 v12, v10, v11
	s_and_saveexec_b64 s[0:1], s[2:3]
	s_cbranch_execz .LBB0_1448
	v_lshl_add_u64 v[14:15], v[8:9], 0, v[2:3]
	v_mov_b32_e32 v13, v245
	v_lshlrev_b32_e32 v14, 16, v13
	v_and_b32_e32 v13, 0xffff0000, v13
	v_mul_f32_e32 v11, v11, v14
	s_waitcnt lgkmcnt(0)
	v_mul_f32_e32 v12, v12, v13
	v_cvt_pk_bf16_f32 v11, v11, v12
	v_lshl_add_u64 v[12:13], v[6:7], 0, v[2:3]
	global_store_dword v[12:13], v11, off offset:64
.LBB0_1448:
	s_or_b64 exec, exec, s[0:1]
	v_mul_f32_e32 v11, v38, v5
	s_waitcnt lgkmcnt(0)
	ds_bpermute_b32 v12, v10, v11
	s_and_saveexec_b64 s[0:1], s[2:3]
	s_cbranch_execz .LBB0_1450
	v_lshl_add_u64 v[14:15], v[8:9], 0, v[2:3]
	v_mov_b32_e32 v13, v246
	v_lshlrev_b32_e32 v14, 16, v13
	v_and_b32_e32 v13, 0xffff0000, v13
	v_mul_f32_e32 v11, v11, v14
	s_waitcnt lgkmcnt(0)
	v_mul_f32_e32 v12, v12, v13
	v_cvt_pk_bf16_f32 v11, v11, v12
	v_lshl_add_u64 v[12:13], v[6:7], 0, v[2:3]
	global_store_dword v[12:13], v11, off offset:128
.LBB0_1450:
	s_or_b64 exec, exec, s[0:1]
	v_mul_f32_e32 v5, v22, v5
	ds_bpermute_b32 v11, v10, v5
	s_and_saveexec_b64 s[0:1], s[2:3]
	s_cbranch_execz .LBB0_1452
	v_lshl_add_u64 v[8:9], v[8:9], 0, v[2:3]
	v_lshl_add_u64 v[6:7], v[6:7], 0, v[2:3]
	v_mov_b32_e32 v8, v247
	v_lshlrev_b32_e32 v9, 16, v8
	v_and_b32_e32 v8, 0xffff0000, v8
	v_mul_f32_e32 v5, v5, v9
	s_waitcnt lgkmcnt(0)
	v_mul_f32_e32 v8, v11, v8
	v_cvt_pk_bf16_f32 v5, v5, v8
	global_store_dword v[6:7], v5, off offset:192
; __device__ __forceinline__ unsigned cvt_pk_bf16(float lo, float hi) { unsigned r; asm volatile("v_cvt_pk_bf16_f32 %0, %1, %2" : "=v"(r) : "v"(lo), "v"(hi)); return r; }
; __device__ __forceinline__ float bf_lo(unsigned w) { return __uint_as_float(w << 16); }
; __device__ __forceinline__ float bf_hi(unsigned w) { return __uint_as_float(w & 0xffff0000u); }
; __device__ __forceinline__ int crow(int r, int hi) { return (r & 3) + 8 * (r >> 2) + 4 * hi; }
; template <int MODE> ...
;     ...
;     if (hi == 0) li_l[r32] = l_reg; asm volatile("s_waitcnt lgkmcnt(0)" ::: "memory");
; #pragma unroll
;     for (int r = 0; r < 16; ++r) { const int orow = qlo + crow(r, hi); const float rl = __builtin_amdgcn_rcpf(li_l[crow(r, hi)]);
; #pragma unroll
;         for (int d0 = 0; d0 < 4; ++d0) { float v = o[d0][r] * rl; float vn = __shfl_xor(v, 1);
;             if ((r32 & 1) == 0) { const int col = d0 * 32 + r32;
;                 if (MODE == 1) { const unsigned g = *(const unsigned*)(gate + (size_t)orow * 1024 + hoff + col); v *= bf_lo(g); vn *= bf_hi(g); }
;                 *(unsigned*)(Ob + (size_t)orow * DM + ocol0 + col) = cvt_pk_bf16(v, vn); } } }
.LBB0_1452:
	s_or_b64 exec, exec, s[0:1]
	ds_read_b32 v5, v160 offset:36
	v_add_u32_e32 v6, 9, v4
	v_ashrrev_i32_e32 v7, 31, v6
	v_lshlrev_b64 v[8:9], 11, v[6:7]
	v_lshlrev_b64 v[6:7], 12, v[6:7]
	s_waitcnt lgkmcnt(0)
	v_rcp_f32_e32 v5, v5
	v_lshl_add_u64 v[8:9], s[6:7], 0, v[8:9]
	v_lshl_add_u64 v[6:7], s[8:9], 0, v[6:7]
	v_lshl_add_u64 v[242:243], v[8:9], 0, v[2:3]
	global_load_dword v244, v[242:243], off
	global_load_dword v245, v[242:243], off offset:64
	global_load_dword v246, v[242:243], off offset:128
	global_load_dword v247, v[242:243], off offset:192
	v_mul_f32_e32 v11, v71, v5
	ds_bpermute_b32 v12, v10, v11
	s_and_saveexec_b64 s[0:1], s[2:3]
	s_cbranch_execz .LBB0_1454
	v_lshl_add_u64 v[14:15], v[8:9], 0, v[2:3]
	s_waitcnt vmcnt(0)
	v_mov_b32_e32 v13, v244
	v_lshlrev_b32_e32 v14, 16, v13
	v_and_b32_e32 v13, 0xffff0000, v13
	v_mul_f32_e32 v11, v11, v14
	s_waitcnt lgkmcnt(0)
	v_mul_f32_e32 v12, v12, v13
	v_cvt_pk_bf16_f32 v11, v11, v12
	v_lshl_add_u64 v[12:13], v[6:7], 0, v[2:3]
	global_store_dword v[12:13], v11, off
.LBB0_1454:
	s_or_b64 exec, exec, s[0:1]
	v_mul_f32_e32 v11, v55, v5
	s_waitcnt lgkmcnt(0)
	ds_bpermute_b32 v12, v10, v11
	s_and_saveexec_b64 s[0:1], s[2:3]
	s_cbranch_execz .LBB0_1456
	v_lshl_add_u64 v[14:15], v[8:9], 0, v[2:3]
	v_mov_b32_e32 v13, v245
	v_lshlrev_b32_e32 v14, 16, v13
	v_and_b32_e32 v13, 0xffff0000, v13
	v_mul_f32_e32 v11, v11, v14
	s_waitcnt lgkmcnt(0)
	v_mul_f32_e32 v12, v12, v13
	v_cvt_pk_bf16_f32 v11, v11, v12
	v_lshl_add_u64 v[12:13], v[6:7], 0, v[2:3]
	global_store_dword v[12:13], v11, off offset:64
.LBB0_1456:
	s_or_b64 exec, exec, s[0:1]
	v_mul_f32_e32 v11, v39, v5
	s_waitcnt lgkmcnt(0)
	ds_bpermute_b32 v12, v10, v11
	s_and_saveexec_b64 s[0:1], s[2:3]
	s_cbranch_execz .LBB0_1458
	v_lshl_add_u64 v[14:15], v[8:9], 0, v[2:3]
	v_mov_b32_e32 v13, v246
	v_lshlrev_b32_e32 v14, 16, v13
	v_and_b32_e32 v13, 0xffff0000, v13
	v_mul_f32_e32 v11, v11, v14
	s_waitcnt lgkmcnt(0)
	v_mul_f32_e32 v12, v12, v13
	v_cvt_pk_bf16_f32 v11, v11, v12
	v_lshl_add_u64 v[12:13], v[6:7], 0, v[2:3]
	global_store_dword v[12:13], v11, off offset:128
.LBB0_1458:
	s_or_b64 exec, exec, s[0:1]
	v_mul_f32_e32 v5, v23, v5
	ds_bpermute_b32 v11, v10, v5
	s_and_saveexec_b64 s[0:1], s[2:3]
	s_cbranch_execz .LBB0_1460
	v_lshl_add_u64 v[8:9], v[8:9], 0, v[2:3]
	v_lshl_add_u64 v[6:7], v[6:7], 0, v[2:3]
	v_mov_b32_e32 v8, v247
	v_lshlrev_b32_e32 v9, 16, v8
	v_and_b32_e32 v8, 0xffff0000, v8
	v_mul_f32_e32 v5, v5, v9
	s_waitcnt lgkmcnt(0)
	v_mul_f32_e32 v8, v11, v8
	v_cvt_pk_bf16_f32 v5, v5, v8
	global_store_dword v[6:7], v5, off offset:192
.LBB0_1460:
	s_or_b64 exec, exec, s[0:1]
	ds_read_b32 v5, v160 offset:40
	v_add_u32_e32 v6, 10, v4
	v_ashrrev_i32_e32 v7, 31, v6
	v_lshlrev_b64 v[8:9], 11, v[6:7]
	v_lshlrev_b64 v[6:7], 12, v[6:7]
	s_waitcnt lgkmcnt(0)
	v_rcp_f32_e32 v5, v5
	v_lshl_add_u64 v[8:9], s[6:7], 0, v[8:9]
	v_lshl_add_u64 v[6:7], s[8:9], 0, v[6:7]
	v_lshl_add_u64 v[242:243], v[8:9], 0, v[2:3]
	global_load_dword v244, v[242:243], off
	global_load_dword v245, v[242:243], off offset:64
	global_load_dword v246, v[242:243], off offset:128
	global_load_dword v247, v[242:243], off offset:192
	v_mul_f32_e32 v11, v72, v5
	ds_bpermute_b32 v12, v10, v11
	s_and_saveexec_b64 s[0:1], s[2:3]
	s_cbranch_execz .LBB0_1462
	v_lshl_add_u64 v[14:15], v[8:9], 0, v[2:3]
	s_waitcnt vmcnt(0)
	v_mov_b32_e32 v13, v244
	v_lshlrev_b32_e32 v14, 16, v13
	v_and_b32_e32 v13, 0xffff0000, v13
	v_mul_f32_e32 v11, v11, v14
	s_waitcnt lgkmcnt(0)
	v_mul_f32_e32 v12, v12, v13
	v_cvt_pk_bf16_f32 v11, v11, v12
	v_lshl_add_u64 v[12:13], v[6:7], 0, v[2:3]
	global_store_dword v[12:13], v11, off
.LBB0_1462:
	s_or_b64 exec, exec, s[0:1]
	v_mul_f32_e32 v11, v56, v5
	s_waitcnt lgkmcnt(0)
	ds_bpermute_b32 v12, v10, v11
	s_and_saveexec_b64 s[0:1], s[2:3]
	s_cbranch_execz .LBB0_1464
	v_lshl_add_u64 v[14:15], v[8:9], 0, v[2:3]
	v_mov_b32_e32 v13, v245
	v_lshlrev_b32_e32 v14, 16, v13
	v_and_b32_e32 v13, 0xffff0000, v13
	v_mul_f32_e32 v11, v11, v14
	s_waitcnt lgkmcnt(0)
	v_mul_f32_e32 v12, v12, v13
	v_cvt_pk_bf16_f32 v11, v11, v12
	v_lshl_add_u64 v[12:13], v[6:7], 0, v[2:3]
	global_store_dword v[12:13], v11, off offset:64
.LBB0_1464:
	s_or_b64 exec, exec, s[0:1]
	v_mul_f32_e32 v11, v40, v5
	s_waitcnt lgkmcnt(0)
	ds_bpermute_b32 v12, v10, v11
	s_and_saveexec_b64 s[0:1], s[2:3]
	s_cbranch_execz .LBB0_1466
	v_lshl_add_u64 v[14:15], v[8:9], 0, v[2:3]
	v_mov_b32_e32 v13, v246
	v_lshlrev_b32_e32 v14, 16, v13
	v_and_b32_e32 v13, 0xffff0000, v13
	v_mul_f32_e32 v11, v11, v14
	s_waitcnt lgkmcnt(0)
	v_mul_f32_e32 v12, v12, v13
	v_cvt_pk_bf16_f32 v11, v11, v12
	v_lshl_add_u64 v[12:13], v[6:7], 0, v[2:3]
	global_store_dword v[12:13], v11, off offset:128
.LBB0_1466:
	s_or_b64 exec, exec, s[0:1]
	v_mul_f32_e32 v5, v24, v5
	ds_bpermute_b32 v11, v10, v5
	s_and_saveexec_b64 s[0:1], s[2:3]
	s_cbranch_execz .LBB0_1468
	v_lshl_add_u64 v[8:9], v[8:9], 0, v[2:3]
	v_lshl_add_u64 v[6:7], v[6:7], 0, v[2:3]
	v_mov_b32_e32 v8, v247
	v_lshlrev_b32_e32 v9, 16, v8
	v_and_b32_e32 v8, 0xffff0000, v8
	v_mul_f32_e32 v5, v5, v9
	s_waitcnt lgkmcnt(0)
	v_mul_f32_e32 v8, v11, v8
	v_cvt_pk_bf16_f32 v5, v5, v8
	global_store_dword v[6:7], v5, off offset:192
; __device__ __forceinline__ unsigned cvt_pk_bf16(float lo, float hi) { unsigned r; asm volatile("v_cvt_pk_bf16_f32 %0, %1, %2" : "=v"(r) : "v"(lo), "v"(hi)); return r; }
; __device__ __forceinline__ float bf_lo(unsigned w) { return __uint_as_float(w << 16); }
; __device__ __forceinline__ float bf_hi(unsigned w) { return __uint_as_float(w & 0xffff0000u); }
; __device__ __forceinline__ int crow(int r, int hi) { return (r & 3) + 8 * (r >> 2) + 4 * hi; }
; template <int MODE> ...
;     ...
;     if (hi == 0) li_l[r32] = l_reg; asm volatile("s_waitcnt lgkmcnt(0)" ::: "memory");
; #pragma unroll
;     for (int r = 0; r < 16; ++r) { const int orow = qlo + crow(r, hi); const float rl = __builtin_amdgcn_rcpf(li_l[crow(r, hi)]);
; #pragma unroll
;         for (int d0 = 0; d0 < 4; ++d0) { float v = o[d0][r] * rl; float vn = __shfl_xor(v, 1);
;             if ((r32 & 1) == 0) { const int col = d0 * 32 + r32;
;                 if (MODE == 1) { const unsigned g = *(const unsigned*)(gate + (size_t)orow * 1024 + hoff + col); v *= bf_lo(g); vn *= bf_hi(g); }
;                 *(unsigned*)(Ob + (size_t)orow * DM + ocol0 + col) = cvt_pk_bf16(v, vn); } } }
.LBB0_1468:
	s_or_b64 exec, exec, s[0:1]
	ds_read_b32 v5, v160 offset:44
	v_add_u32_e32 v6, 11, v4
	v_ashrrev_i32_e32 v7, 31, v6
	v_lshlrev_b64 v[8:9], 11, v[6:7]
	v_lshlrev_b64 v[6:7], 12, v[6:7]
	s_waitcnt lgkmcnt(0)
	v_rcp_f32_e32 v5, v5
	v_lshl_add_u64 v[8:9], s[6:7], 0, v[8:9]
	v_lshl_add_u64 v[6:7], s[8:9], 0, v[6:7]
	v_lshl_add_u64 v[242:243], v[8:9], 0, v[2:3]
	global_load_dword v244, v[242:243], off
	global_load_dword v245, v[242:243], off offset:64
	global_load_dword v246, v[242:243], off offset:128
	global_load_dword v247, v[242:243], off offset:192
	v_mul_f32_e32 v11, v73, v5
	ds_bpermute_b32 v12, v10, v11
	s_and_saveexec_b64 s[0:1], s[2:3]
	s_cbranch_execz .LBB0_1470
	v_lshl_add_u64 v[14:15], v[8:9], 0, v[2:3]
	s_waitcnt vmcnt(0)
	v_mov_b32_e32 v13, v244
	v_lshlrev_b32_e32 v14, 16, v13
	v_and_b32_e32 v13, 0xffff0000, v13
	v_mul_f32_e32 v11, v11, v14
	s_waitcnt lgkmcnt(0)
	v_mul_f32_e32 v12, v12, v13
	v_cvt_pk_bf16_f32 v11, v11, v12
	v_lshl_add_u64 v[12:13], v[6:7], 0, v[2:3]
	global_store_dword v[12:13], v11, off
.LBB0_1470:
	s_or_b64 exec, exec, s[0:1]
	v_mul_f32_e32 v11, v57, v5
	s_waitcnt lgkmcnt(0)
	ds_bpermute_b32 v12, v10, v11
	s_and_saveexec_b64 s[0:1], s[2:3]
	s_cbranch_execz .LBB0_1472
	v_lshl_add_u64 v[14:15], v[8:9], 0, v[2:3]
	v_mov_b32_e32 v13, v245
	v_lshlrev_b32_e32 v14, 16, v13
	v_and_b32_e32 v13, 0xffff0000, v13
	v_mul_f32_e32 v11, v11, v14
	s_waitcnt lgkmcnt(0)
	v_mul_f32_e32 v12, v12, v13
	v_cvt_pk_bf16_f32 v11, v11, v12
	v_lshl_add_u64 v[12:13], v[6:7], 0, v[2:3]
	global_store_dword v[12:13], v11, off offset:64
.LBB0_1472:
	s_or_b64 exec, exec, s[0:1]
	v_mul_f32_e32 v11, v41, v5
	s_waitcnt lgkmcnt(0)
	ds_bpermute_b32 v12, v10, v11
	s_and_saveexec_b64 s[0:1], s[2:3]
	s_cbranch_execz .LBB0_1474
	v_lshl_add_u64 v[14:15], v[8:9], 0, v[2:3]
	v_mov_b32_e32 v13, v246
	v_lshlrev_b32_e32 v14, 16, v13
	v_and_b32_e32 v13, 0xffff0000, v13
	v_mul_f32_e32 v11, v11, v14
	s_waitcnt lgkmcnt(0)
	v_mul_f32_e32 v12, v12, v13
	v_cvt_pk_bf16_f32 v11, v11, v12
	v_lshl_add_u64 v[12:13], v[6:7], 0, v[2:3]
	global_store_dword v[12:13], v11, off offset:128
.LBB0_1474:
	s_or_b64 exec, exec, s[0:1]
	v_mul_f32_e32 v5, v25, v5
	ds_bpermute_b32 v11, v10, v5
	s_and_saveexec_b64 s[0:1], s[2:3]
	s_cbranch_execz .LBB0_1476
	v_lshl_add_u64 v[8:9], v[8:9], 0, v[2:3]
	v_lshl_add_u64 v[6:7], v[6:7], 0, v[2:3]
	v_mov_b32_e32 v8, v247
	v_lshlrev_b32_e32 v9, 16, v8
	v_and_b32_e32 v8, 0xffff0000, v8
	v_mul_f32_e32 v5, v5, v9
	s_waitcnt lgkmcnt(0)
	v_mul_f32_e32 v8, v11, v8
	v_cvt_pk_bf16_f32 v5, v5, v8
	global_store_dword v[6:7], v5, off offset:192
.LBB0_1476:
	s_or_b64 exec, exec, s[0:1]
	ds_read_b32 v5, v160 offset:64
	v_add_u32_e32 v6, 16, v4
	v_ashrrev_i32_e32 v7, 31, v6
	v_lshlrev_b64 v[8:9], 11, v[6:7]
	v_lshlrev_b64 v[6:7], 12, v[6:7]
	s_waitcnt lgkmcnt(0)
	v_rcp_f32_e32 v5, v5
	v_lshl_add_u64 v[8:9], s[6:7], 0, v[8:9]
	v_lshl_add_u64 v[6:7], s[8:9], 0, v[6:7]
	v_lshl_add_u64 v[242:243], v[8:9], 0, v[2:3]
	global_load_dword v244, v[242:243], off
	global_load_dword v245, v[242:243], off offset:64
	global_load_dword v246, v[242:243], off offset:128
	global_load_dword v247, v[242:243], off offset:192
	v_mul_f32_e32 v11, v74, v5
	ds_bpermute_b32 v12, v10, v11
	s_and_saveexec_b64 s[0:1], s[2:3]
	s_cbranch_execz .LBB0_1478
	v_lshl_add_u64 v[14:15], v[8:9], 0, v[2:3]
	s_waitcnt vmcnt(0)
	v_mov_b32_e32 v13, v244
	v_lshlrev_b32_e32 v14, 16, v13
	v_and_b32_e32 v13, 0xffff0000, v13
	v_mul_f32_e32 v11, v11, v14
	s_waitcnt lgkmcnt(0)
	v_mul_f32_e32 v12, v12, v13
	v_cvt_pk_bf16_f32 v11, v11, v12
	v_lshl_add_u64 v[12:13], v[6:7], 0, v[2:3]
	global_store_dword v[12:13], v11, off
.LBB0_1478:
	s_or_b64 exec, exec, s[0:1]
	v_mul_f32_e32 v11, v58, v5
	s_waitcnt lgkmcnt(0)
	ds_bpermute_b32 v12, v10, v11
	s_and_saveexec_b64 s[0:1], s[2:3]
	s_cbranch_execz .LBB0_1480
	v_lshl_add_u64 v[14:15], v[8:9], 0, v[2:3]
	v_mov_b32_e32 v13, v245
	v_lshlrev_b32_e32 v14, 16, v13
	v_and_b32_e32 v13, 0xffff0000, v13
	v_mul_f32_e32 v11, v11, v14
	s_waitcnt lgkmcnt(0)
	v_mul_f32_e32 v12, v12, v13
	v_cvt_pk_bf16_f32 v11, v11, v12
	v_lshl_add_u64 v[12:13], v[6:7], 0, v[2:3]
	global_store_dword v[12:13], v11, off offset:64
.LBB0_1480:
	s_or_b64 exec, exec, s[0:1]
	v_mul_f32_e32 v11, v42, v5
	s_waitcnt lgkmcnt(0)
	ds_bpermute_b32 v12, v10, v11
	s_and_saveexec_b64 s[0:1], s[2:3]
	s_cbranch_execz .LBB0_1482
	v_lshl_add_u64 v[14:15], v[8:9], 0, v[2:3]
	v_mov_b32_e32 v13, v246
	v_lshlrev_b32_e32 v14, 16, v13
	v_and_b32_e32 v13, 0xffff0000, v13
	v_mul_f32_e32 v11, v11, v14
	s_waitcnt lgkmcnt(0)
	v_mul_f32_e32 v12, v12, v13
	v_cvt_pk_bf16_f32 v11, v11, v12
	v_lshl_add_u64 v[12:13], v[6:7], 0, v[2:3]
	global_store_dword v[12:13], v11, off offset:128
.LBB0_1482:
	s_or_b64 exec, exec, s[0:1]
	v_mul_f32_e32 v5, v26, v5
	ds_bpermute_b32 v11, v10, v5
	s_and_saveexec_b64 s[0:1], s[2:3]
	s_cbranch_execz .LBB0_1484
	v_lshl_add_u64 v[8:9], v[8:9], 0, v[2:3]
	v_lshl_add_u64 v[6:7], v[6:7], 0, v[2:3]
	v_mov_b32_e32 v8, v247
	v_lshlrev_b32_e32 v9, 16, v8
	v_and_b32_e32 v8, 0xffff0000, v8
	v_mul_f32_e32 v5, v5, v9
	s_waitcnt lgkmcnt(0)
	v_mul_f32_e32 v8, v11, v8
	v_cvt_pk_bf16_f32 v5, v5, v8
	global_store_dword v[6:7], v5, off offset:192
; __device__ __forceinline__ unsigned cvt_pk_bf16(float lo, float hi) { unsigned r; asm volatile("v_cvt_pk_bf16_f32 %0, %1, %2" : "=v"(r) : "v"(lo), "v"(hi)); return r; }
; __device__ __forceinline__ float bf_lo(unsigned w) { return __uint_as_float(w << 16); }
; __device__ __forceinline__ float bf_hi(unsigned w) { return __uint_as_float(w & 0xffff0000u); }
; __device__ __forceinline__ int crow(int r, int hi) { return (r & 3) + 8 * (r >> 2) + 4 * hi; }
; template <int MODE> ...
;     ...
;     if (hi == 0) li_l[r32] = l_reg; asm volatile("s_waitcnt lgkmcnt(0)" ::: "memory");
; #pragma unroll
;     for (int r = 0; r < 16; ++r) { const int orow = qlo + crow(r, hi); const float rl = __builtin_amdgcn_rcpf(li_l[crow(r, hi)]);
; #pragma unroll
;         for (int d0 = 0; d0 < 4; ++d0) { float v = o[d0][r] * rl; float vn = __shfl_xor(v, 1);
;             if ((r32 & 1) == 0) { const int col = d0 * 32 + r32;
;                 if (MODE == 1) { const unsigned g = *(const unsigned*)(gate + (size_t)orow * 1024 + hoff + col); v *= bf_lo(g); vn *= bf_hi(g); }
;                 *(unsigned*)(Ob + (size_t)orow * DM + ocol0 + col) = cvt_pk_bf16(v, vn); } } }
.LBB0_1484:
	s_or_b64 exec, exec, s[0:1]
	ds_read_b32 v5, v160 offset:68
	v_add_u32_e32 v6, 17, v4
	v_ashrrev_i32_e32 v7, 31, v6
	v_lshlrev_b64 v[8:9], 11, v[6:7]
	v_lshlrev_b64 v[6:7], 12, v[6:7]
	s_waitcnt lgkmcnt(0)
	v_rcp_f32_e32 v5, v5
	v_lshl_add_u64 v[8:9], s[6:7], 0, v[8:9]
	v_lshl_add_u64 v[6:7], s[8:9], 0, v[6:7]
	v_lshl_add_u64 v[242:243], v[8:9], 0, v[2:3]
	global_load_dword v244, v[242:243], off
	global_load_dword v245, v[242:243], off offset:64
	global_load_dword v246, v[242:243], off offset:128
	global_load_dword v247, v[242:243], off offset:192
	v_mul_f32_e32 v11, v75, v5
	ds_bpermute_b32 v12, v10, v11
	s_and_saveexec_b64 s[0:1], s[2:3]
	s_cbranch_execz .LBB0_1486
	v_lshl_add_u64 v[14:15], v[8:9], 0, v[2:3]
	s_waitcnt vmcnt(0)
	v_mov_b32_e32 v13, v244
	v_lshlrev_b32_e32 v14, 16, v13
	v_and_b32_e32 v13, 0xffff0000, v13
	v_mul_f32_e32 v11, v11, v14
	s_waitcnt lgkmcnt(0)
	v_mul_f32_e32 v12, v12, v13
	v_cvt_pk_bf16_f32 v11, v11, v12
	v_lshl_add_u64 v[12:13], v[6:7], 0, v[2:3]
	global_store_dword v[12:13], v11, off
.LBB0_1486:
	s_or_b64 exec, exec, s[0:1]
	v_mul_f32_e32 v11, v59, v5
	s_waitcnt lgkmcnt(0)
	ds_bpermute_b32 v12, v10, v11
	s_and_saveexec_b64 s[0:1], s[2:3]
	s_cbranch_execz .LBB0_1488
	v_lshl_add_u64 v[14:15], v[8:9], 0, v[2:3]
	v_mov_b32_e32 v13, v245
	v_lshlrev_b32_e32 v14, 16, v13
	v_and_b32_e32 v13, 0xffff0000, v13
	v_mul_f32_e32 v11, v11, v14
	s_waitcnt lgkmcnt(0)
	v_mul_f32_e32 v12, v12, v13
	v_cvt_pk_bf16_f32 v11, v11, v12
	v_lshl_add_u64 v[12:13], v[6:7], 0, v[2:3]
	global_store_dword v[12:13], v11, off offset:64
.LBB0_1488:
	s_or_b64 exec, exec, s[0:1]
	v_mul_f32_e32 v11, v43, v5
	s_waitcnt lgkmcnt(0)
	ds_bpermute_b32 v12, v10, v11
	s_and_saveexec_b64 s[0:1], s[2:3]
	s_cbranch_execz .LBB0_1490
	v_lshl_add_u64 v[14:15], v[8:9], 0, v[2:3]
	v_mov_b32_e32 v13, v246
	v_lshlrev_b32_e32 v14, 16, v13
	v_and_b32_e32 v13, 0xffff0000, v13
	v_mul_f32_e32 v11, v11, v14
	s_waitcnt lgkmcnt(0)
	v_mul_f32_e32 v12, v12, v13
	v_cvt_pk_bf16_f32 v11, v11, v12
	v_lshl_add_u64 v[12:13], v[6:7], 0, v[2:3]
	global_store_dword v[12:13], v11, off offset:128
.LBB0_1490:
	s_or_b64 exec, exec, s[0:1]
	v_mul_f32_e32 v5, v27, v5
	ds_bpermute_b32 v11, v10, v5
	s_and_saveexec_b64 s[0:1], s[2:3]
	s_cbranch_execz .LBB0_1492
	v_lshl_add_u64 v[8:9], v[8:9], 0, v[2:3]
	v_lshl_add_u64 v[6:7], v[6:7], 0, v[2:3]
	v_mov_b32_e32 v8, v247
	v_lshlrev_b32_e32 v9, 16, v8
	v_and_b32_e32 v8, 0xffff0000, v8
	v_mul_f32_e32 v5, v5, v9
	s_waitcnt lgkmcnt(0)
	v_mul_f32_e32 v8, v11, v8
	v_cvt_pk_bf16_f32 v5, v5, v8
	global_store_dword v[6:7], v5, off offset:192
.LBB0_1492:
	s_or_b64 exec, exec, s[0:1]
	ds_read_b32 v5, v160 offset:72
	v_add_u32_e32 v6, 18, v4
	v_ashrrev_i32_e32 v7, 31, v6
	v_lshlrev_b64 v[8:9], 11, v[6:7]
	v_lshlrev_b64 v[6:7], 12, v[6:7]
	s_waitcnt lgkmcnt(0)
	v_rcp_f32_e32 v5, v5
	v_lshl_add_u64 v[8:9], s[6:7], 0, v[8:9]
	v_lshl_add_u64 v[6:7], s[8:9], 0, v[6:7]
	v_lshl_add_u64 v[242:243], v[8:9], 0, v[2:3]
	global_load_dword v244, v[242:243], off
	global_load_dword v245, v[242:243], off offset:64
	global_load_dword v246, v[242:243], off offset:128
	global_load_dword v247, v[242:243], off offset:192
	v_mul_f32_e32 v11, v76, v5
	ds_bpermute_b32 v12, v10, v11
	s_and_saveexec_b64 s[0:1], s[2:3]
	s_cbranch_execz .LBB0_1494
	v_lshl_add_u64 v[14:15], v[8:9], 0, v[2:3]
	s_waitcnt vmcnt(0)
	v_mov_b32_e32 v13, v244
	v_lshlrev_b32_e32 v14, 16, v13
	v_and_b32_e32 v13, 0xffff0000, v13
	v_mul_f32_e32 v11, v11, v14
	s_waitcnt lgkmcnt(0)
	v_mul_f32_e32 v12, v12, v13
	v_cvt_pk_bf16_f32 v11, v11, v12
	v_lshl_add_u64 v[12:13], v[6:7], 0, v[2:3]
	global_store_dword v[12:13], v11, off
.LBB0_1494:
	s_or_b64 exec, exec, s[0:1]
	v_mul_f32_e32 v11, v60, v5
	s_waitcnt lgkmcnt(0)
	ds_bpermute_b32 v12, v10, v11
	s_and_saveexec_b64 s[0:1], s[2:3]
	s_cbranch_execz .LBB0_1496
	v_lshl_add_u64 v[14:15], v[8:9], 0, v[2:3]
	v_mov_b32_e32 v13, v245
	v_lshlrev_b32_e32 v14, 16, v13
	v_and_b32_e32 v13, 0xffff0000, v13
	v_mul_f32_e32 v11, v11, v14
	s_waitcnt lgkmcnt(0)
	v_mul_f32_e32 v12, v12, v13
	v_cvt_pk_bf16_f32 v11, v11, v12
	v_lshl_add_u64 v[12:13], v[6:7], 0, v[2:3]
	global_store_dword v[12:13], v11, off offset:64
.LBB0_1496:
	s_or_b64 exec, exec, s[0:1]
	v_mul_f32_e32 v11, v44, v5
	s_waitcnt lgkmcnt(0)
	ds_bpermute_b32 v12, v10, v11
	s_and_saveexec_b64 s[0:1], s[2:3]
	s_cbranch_execz .LBB0_1498
	v_lshl_add_u64 v[14:15], v[8:9], 0, v[2:3]
	v_mov_b32_e32 v13, v246
	v_lshlrev_b32_e32 v14, 16, v13
	v_and_b32_e32 v13, 0xffff0000, v13
	v_mul_f32_e32 v11, v11, v14
	s_waitcnt lgkmcnt(0)
	v_mul_f32_e32 v12, v12, v13
	v_cvt_pk_bf16_f32 v11, v11, v12
	v_lshl_add_u64 v[12:13], v[6:7], 0, v[2:3]
	global_store_dword v[12:13], v11, off offset:128
.LBB0_1498:
	s_or_b64 exec, exec, s[0:1]
	v_mul_f32_e32 v5, v28, v5
	ds_bpermute_b32 v11, v10, v5
	s_and_saveexec_b64 s[0:1], s[2:3]
	s_cbranch_execz .LBB0_1500
	v_lshl_add_u64 v[8:9], v[8:9], 0, v[2:3]
	v_lshl_add_u64 v[6:7], v[6:7], 0, v[2:3]
	v_mov_b32_e32 v8, v247
	v_lshlrev_b32_e32 v9, 16, v8
	v_and_b32_e32 v8, 0xffff0000, v8
	v_mul_f32_e32 v5, v5, v9
	s_waitcnt lgkmcnt(0)
	v_mul_f32_e32 v8, v11, v8
	v_cvt_pk_bf16_f32 v5, v5, v8
	global_store_dword v[6:7], v5, off offset:192
; __device__ __forceinline__ unsigned cvt_pk_bf16(float lo, float hi) { unsigned r; asm volatile("v_cvt_pk_bf16_f32 %0, %1, %2" : "=v"(r) : "v"(lo), "v"(hi)); return r; }
; __device__ __forceinline__ float bf_lo(unsigned w) { return __uint_as_float(w << 16); }
; __device__ __forceinline__ float bf_hi(unsigned w) { return __uint_as_float(w & 0xffff0000u); }
; __device__ __forceinline__ int crow(int r, int hi) { return (r & 3) + 8 * (r >> 2) + 4 * hi; }
; template <int MODE> ...
;     ...
;     if (hi == 0) li_l[r32] = l_reg; asm volatile("s_waitcnt lgkmcnt(0)" ::: "memory");
; #pragma unroll
;     for (int r = 0; r < 16; ++r) { const int orow = qlo + crow(r, hi); const float rl = __builtin_amdgcn_rcpf(li_l[crow(r, hi)]);
; #pragma unroll
;         for (int d0 = 0; d0 < 4; ++d0) { float v = o[d0][r] * rl; float vn = __shfl_xor(v, 1);
;             if ((r32 & 1) == 0) { const int col = d0 * 32 + r32;
;                 if (MODE == 1) { const unsigned g = *(const unsigned*)(gate + (size_t)orow * 1024 + hoff + col); v *= bf_lo(g); vn *= bf_hi(g); }
;                 *(unsigned*)(Ob + (size_t)orow * DM + ocol0 + col) = cvt_pk_bf16(v, vn); } } }
.LBB0_1500:
	s_or_b64 exec, exec, s[0:1]
	ds_read_b32 v5, v160 offset:76
	v_add_u32_e32 v6, 19, v4
	v_ashrrev_i32_e32 v7, 31, v6
	v_lshlrev_b64 v[8:9], 11, v[6:7]
	v_lshlrev_b64 v[6:7], 12, v[6:7]
	s_waitcnt lgkmcnt(0)
	v_rcp_f32_e32 v5, v5
	v_lshl_add_u64 v[8:9], s[6:7], 0, v[8:9]
	v_lshl_add_u64 v[6:7], s[8:9], 0, v[6:7]
	v_lshl_add_u64 v[242:243], v[8:9], 0, v[2:3]
	global_load_dword v244, v[242:243], off
	global_load_dword v245, v[242:243], off offset:64
	global_load_dword v246, v[242:243], off offset:128
	global_load_dword v247, v[242:243], off offset:192
	v_mul_f32_e32 v11, v77, v5
	ds_bpermute_b32 v12, v10, v11
	s_and_saveexec_b64 s[0:1], s[2:3]
	s_cbranch_execz .LBB0_1502
	v_lshl_add_u64 v[14:15], v[8:9], 0, v[2:3]
	s_waitcnt vmcnt(0)
	v_mov_b32_e32 v13, v244
	v_lshlrev_b32_e32 v14, 16, v13
	v_and_b32_e32 v13, 0xffff0000, v13
	v_mul_f32_e32 v11, v11, v14
	s_waitcnt lgkmcnt(0)
	v_mul_f32_e32 v12, v12, v13
	v_cvt_pk_bf16_f32 v11, v11, v12
	v_lshl_add_u64 v[12:13], v[6:7], 0, v[2:3]
	global_store_dword v[12:13], v11, off
.LBB0_1502:
	s_or_b64 exec, exec, s[0:1]
	v_mul_f32_e32 v11, v61, v5
	s_waitcnt lgkmcnt(0)
	ds_bpermute_b32 v12, v10, v11
	s_and_saveexec_b64 s[0:1], s[2:3]
	s_cbranch_execz .LBB0_1504
	v_lshl_add_u64 v[14:15], v[8:9], 0, v[2:3]
	v_mov_b32_e32 v13, v245
	v_lshlrev_b32_e32 v14, 16, v13
	v_and_b32_e32 v13, 0xffff0000, v13
	v_mul_f32_e32 v11, v11, v14
	s_waitcnt lgkmcnt(0)
	v_mul_f32_e32 v12, v12, v13
	v_cvt_pk_bf16_f32 v11, v11, v12
	v_lshl_add_u64 v[12:13], v[6:7], 0, v[2:3]
	global_store_dword v[12:13], v11, off offset:64
.LBB0_1504:
	s_or_b64 exec, exec, s[0:1]
	v_mul_f32_e32 v11, v45, v5
	s_waitcnt lgkmcnt(0)
	ds_bpermute_b32 v12, v10, v11
	s_and_saveexec_b64 s[0:1], s[2:3]
	s_cbranch_execz .LBB0_1506
	v_lshl_add_u64 v[14:15], v[8:9], 0, v[2:3]
	v_mov_b32_e32 v13, v246
	v_lshlrev_b32_e32 v14, 16, v13
	v_and_b32_e32 v13, 0xffff0000, v13
	v_mul_f32_e32 v11, v11, v14
	s_waitcnt lgkmcnt(0)
	v_mul_f32_e32 v12, v12, v13
	v_cvt_pk_bf16_f32 v11, v11, v12
	v_lshl_add_u64 v[12:13], v[6:7], 0, v[2:3]
	global_store_dword v[12:13], v11, off offset:128
.LBB0_1506:
	s_or_b64 exec, exec, s[0:1]
	v_mul_f32_e32 v5, v29, v5
	ds_bpermute_b32 v11, v10, v5
	s_and_saveexec_b64 s[0:1], s[2:3]
	s_cbranch_execz .LBB0_1508
	v_lshl_add_u64 v[8:9], v[8:9], 0, v[2:3]
	v_lshl_add_u64 v[6:7], v[6:7], 0, v[2:3]
	v_mov_b32_e32 v8, v247
	v_lshlrev_b32_e32 v9, 16, v8
	v_and_b32_e32 v8, 0xffff0000, v8
	v_mul_f32_e32 v5, v5, v9
	s_waitcnt lgkmcnt(0)
	v_mul_f32_e32 v8, v11, v8
	v_cvt_pk_bf16_f32 v5, v5, v8
	global_store_dword v[6:7], v5, off offset:192
.LBB0_1508:
	s_or_b64 exec, exec, s[0:1]
	ds_read_b32 v5, v160 offset:96
	v_add_u32_e32 v6, 24, v4
	v_ashrrev_i32_e32 v7, 31, v6
	v_lshlrev_b64 v[8:9], 11, v[6:7]
	v_lshlrev_b64 v[6:7], 12, v[6:7]
	s_waitcnt lgkmcnt(0)
	v_rcp_f32_e32 v5, v5
	v_lshl_add_u64 v[8:9], s[6:7], 0, v[8:9]
	v_lshl_add_u64 v[6:7], s[8:9], 0, v[6:7]
	v_lshl_add_u64 v[242:243], v[8:9], 0, v[2:3]
	global_load_dword v244, v[242:243], off
	global_load_dword v245, v[242:243], off offset:64
	global_load_dword v246, v[242:243], off offset:128
	global_load_dword v247, v[242:243], off offset:192
	v_mul_f32_e32 v11, v78, v5
	ds_bpermute_b32 v12, v10, v11
	s_and_saveexec_b64 s[0:1], s[2:3]
	s_cbranch_execz .LBB0_1510
	v_lshl_add_u64 v[14:15], v[8:9], 0, v[2:3]
	s_waitcnt vmcnt(0)
	v_mov_b32_e32 v13, v244
	v_lshlrev_b32_e32 v14, 16, v13
	v_and_b32_e32 v13, 0xffff0000, v13
	v_mul_f32_e32 v11, v11, v14
	s_waitcnt lgkmcnt(0)
	v_mul_f32_e32 v12, v12, v13
	v_cvt_pk_bf16_f32 v11, v11, v12
	v_lshl_add_u64 v[12:13], v[6:7], 0, v[2:3]
	global_store_dword v[12:13], v11, off
.LBB0_1510:
	s_or_b64 exec, exec, s[0:1]
	v_mul_f32_e32 v11, v62, v5
	s_waitcnt lgkmcnt(0)
	ds_bpermute_b32 v12, v10, v11
	s_and_saveexec_b64 s[0:1], s[2:3]
	s_cbranch_execz .LBB0_1512
	v_lshl_add_u64 v[14:15], v[8:9], 0, v[2:3]
	v_mov_b32_e32 v13, v245
	v_lshlrev_b32_e32 v14, 16, v13
	v_and_b32_e32 v13, 0xffff0000, v13
	v_mul_f32_e32 v11, v11, v14
	s_waitcnt lgkmcnt(0)
	v_mul_f32_e32 v12, v12, v13
	v_cvt_pk_bf16_f32 v11, v11, v12
	v_lshl_add_u64 v[12:13], v[6:7], 0, v[2:3]
	global_store_dword v[12:13], v11, off offset:64
.LBB0_1512:
	s_or_b64 exec, exec, s[0:1]
	v_mul_f32_e32 v11, v46, v5
	s_waitcnt lgkmcnt(0)
	ds_bpermute_b32 v12, v10, v11
	s_and_saveexec_b64 s[0:1], s[2:3]
	s_cbranch_execz .LBB0_1514
	v_lshl_add_u64 v[14:15], v[8:9], 0, v[2:3]
	v_mov_b32_e32 v13, v246
	v_lshlrev_b32_e32 v14, 16, v13
	v_and_b32_e32 v13, 0xffff0000, v13
	v_mul_f32_e32 v11, v11, v14
	s_waitcnt lgkmcnt(0)
	v_mul_f32_e32 v12, v12, v13
	v_cvt_pk_bf16_f32 v11, v11, v12
	v_lshl_add_u64 v[12:13], v[6:7], 0, v[2:3]
	global_store_dword v[12:13], v11, off offset:128
.LBB0_1514:
	s_or_b64 exec, exec, s[0:1]
	v_mul_f32_e32 v5, v30, v5
	ds_bpermute_b32 v11, v10, v5
	s_and_saveexec_b64 s[0:1], s[2:3]
	s_cbranch_execz .LBB0_1516
	v_lshl_add_u64 v[8:9], v[8:9], 0, v[2:3]
	v_lshl_add_u64 v[6:7], v[6:7], 0, v[2:3]
	v_mov_b32_e32 v8, v247
	v_lshlrev_b32_e32 v9, 16, v8
	v_and_b32_e32 v8, 0xffff0000, v8
	v_mul_f32_e32 v5, v5, v9
	s_waitcnt lgkmcnt(0)
	v_mul_f32_e32 v8, v11, v8
	v_cvt_pk_bf16_f32 v5, v5, v8
	global_store_dword v[6:7], v5, off offset:192
; __device__ __forceinline__ unsigned cvt_pk_bf16(float lo, float hi) { unsigned r; asm volatile("v_cvt_pk_bf16_f32 %0, %1, %2" : "=v"(r) : "v"(lo), "v"(hi)); return r; }
; __device__ __forceinline__ float bf_lo(unsigned w) { return __uint_as_float(w << 16); }
; __device__ __forceinline__ float bf_hi(unsigned w) { return __uint_as_float(w & 0xffff0000u); }
; __device__ __forceinline__ int crow(int r, int hi) { return (r & 3) + 8 * (r >> 2) + 4 * hi; }
; template <int MODE> ...
;     ...
;     if (hi == 0) li_l[r32] = l_reg; asm volatile("s_waitcnt lgkmcnt(0)" ::: "memory");
; #pragma unroll
;     for (int r = 0; r < 16; ++r) { const int orow = qlo + crow(r, hi); const float rl = __builtin_amdgcn_rcpf(li_l[crow(r, hi)]);
; #pragma unroll
;         for (int d0 = 0; d0 < 4; ++d0) { float v = o[d0][r] * rl; float vn = __shfl_xor(v, 1);
;             if ((r32 & 1) == 0) { const int col = d0 * 32 + r32;
;                 if (MODE == 1) { const unsigned g = *(const unsigned*)(gate + (size_t)orow * 1024 + hoff + col); v *= bf_lo(g); vn *= bf_hi(g); }
;                 *(unsigned*)(Ob + (size_t)orow * DM + ocol0 + col) = cvt_pk_bf16(v, vn); } } }
.LBB0_1516:
	s_or_b64 exec, exec, s[0:1]
	ds_read_b32 v5, v160 offset:100
	v_add_u32_e32 v6, 25, v4
	v_ashrrev_i32_e32 v7, 31, v6
	v_lshlrev_b64 v[8:9], 11, v[6:7]
	v_lshlrev_b64 v[6:7], 12, v[6:7]
	s_waitcnt lgkmcnt(0)
	v_rcp_f32_e32 v5, v5
	v_lshl_add_u64 v[8:9], s[6:7], 0, v[8:9]
	v_lshl_add_u64 v[6:7], s[8:9], 0, v[6:7]
	v_lshl_add_u64 v[242:243], v[8:9], 0, v[2:3]
	global_load_dword v244, v[242:243], off
	global_load_dword v245, v[242:243], off offset:64
	global_load_dword v246, v[242:243], off offset:128
	global_load_dword v247, v[242:243], off offset:192
	v_mul_f32_e32 v11, v79, v5
	ds_bpermute_b32 v12, v10, v11
	s_and_saveexec_b64 s[0:1], s[2:3]
	s_cbranch_execz .LBB0_1518
	v_lshl_add_u64 v[14:15], v[8:9], 0, v[2:3]
	s_waitcnt vmcnt(0)
	v_mov_b32_e32 v13, v244
	v_lshlrev_b32_e32 v14, 16, v13
	v_and_b32_e32 v13, 0xffff0000, v13
	v_mul_f32_e32 v11, v11, v14
	s_waitcnt lgkmcnt(0)
	v_mul_f32_e32 v12, v12, v13
	v_cvt_pk_bf16_f32 v11, v11, v12
	v_lshl_add_u64 v[12:13], v[6:7], 0, v[2:3]
	global_store_dword v[12:13], v11, off
.LBB0_1518:
	s_or_b64 exec, exec, s[0:1]
	v_mul_f32_e32 v11, v63, v5
	s_waitcnt lgkmcnt(0)
	ds_bpermute_b32 v12, v10, v11
	s_and_saveexec_b64 s[0:1], s[2:3]
	s_cbranch_execz .LBB0_1520
	v_lshl_add_u64 v[14:15], v[8:9], 0, v[2:3]
	v_mov_b32_e32 v13, v245
	v_lshlrev_b32_e32 v14, 16, v13
	v_and_b32_e32 v13, 0xffff0000, v13
	v_mul_f32_e32 v11, v11, v14
	s_waitcnt lgkmcnt(0)
	v_mul_f32_e32 v12, v12, v13
	v_cvt_pk_bf16_f32 v11, v11, v12
	v_lshl_add_u64 v[12:13], v[6:7], 0, v[2:3]
	global_store_dword v[12:13], v11, off offset:64
.LBB0_1520:
	s_or_b64 exec, exec, s[0:1]
	v_mul_f32_e32 v11, v47, v5
	s_waitcnt lgkmcnt(0)
	ds_bpermute_b32 v12, v10, v11
	s_and_saveexec_b64 s[0:1], s[2:3]
	s_cbranch_execz .LBB0_1522
	v_lshl_add_u64 v[14:15], v[8:9], 0, v[2:3]
	v_mov_b32_e32 v13, v246
	v_lshlrev_b32_e32 v14, 16, v13
	v_and_b32_e32 v13, 0xffff0000, v13
	v_mul_f32_e32 v11, v11, v14
	s_waitcnt lgkmcnt(0)
	v_mul_f32_e32 v12, v12, v13
	v_cvt_pk_bf16_f32 v11, v11, v12
	v_lshl_add_u64 v[12:13], v[6:7], 0, v[2:3]
	global_store_dword v[12:13], v11, off offset:128
.LBB0_1522:
	s_or_b64 exec, exec, s[0:1]
	v_mul_f32_e32 v5, v31, v5
	ds_bpermute_b32 v11, v10, v5
	s_and_saveexec_b64 s[0:1], s[2:3]
	s_cbranch_execz .LBB0_1524
	v_lshl_add_u64 v[8:9], v[8:9], 0, v[2:3]
	v_lshl_add_u64 v[6:7], v[6:7], 0, v[2:3]
	v_mov_b32_e32 v8, v247
	v_lshlrev_b32_e32 v9, 16, v8
	v_and_b32_e32 v8, 0xffff0000, v8
	v_mul_f32_e32 v5, v5, v9
	s_waitcnt lgkmcnt(0)
	v_mul_f32_e32 v8, v11, v8
	v_cvt_pk_bf16_f32 v5, v5, v8
	global_store_dword v[6:7], v5, off offset:192
.LBB0_1524:
	s_or_b64 exec, exec, s[0:1]
	ds_read_b32 v5, v160 offset:104
	v_add_u32_e32 v6, 26, v4
	v_ashrrev_i32_e32 v7, 31, v6
	v_lshlrev_b64 v[8:9], 11, v[6:7]
	v_lshlrev_b64 v[6:7], 12, v[6:7]
	s_waitcnt lgkmcnt(0)
	v_rcp_f32_e32 v5, v5
	v_lshl_add_u64 v[8:9], s[6:7], 0, v[8:9]
	v_lshl_add_u64 v[6:7], s[8:9], 0, v[6:7]
	v_lshl_add_u64 v[242:243], v[8:9], 0, v[2:3]
	global_load_dword v244, v[242:243], off
	global_load_dword v245, v[242:243], off offset:64
	global_load_dword v246, v[242:243], off offset:128
	global_load_dword v247, v[242:243], off offset:192
	v_mul_f32_e32 v11, v80, v5
	ds_bpermute_b32 v12, v10, v11
	s_and_saveexec_b64 s[0:1], s[2:3]
	s_cbranch_execz .LBB0_1526
	v_lshl_add_u64 v[14:15], v[8:9], 0, v[2:3]
	s_waitcnt vmcnt(0)
	v_mov_b32_e32 v13, v244
	v_lshlrev_b32_e32 v14, 16, v13
	v_and_b32_e32 v13, 0xffff0000, v13
	v_mul_f32_e32 v11, v11, v14
	s_waitcnt lgkmcnt(0)
	v_mul_f32_e32 v12, v12, v13
	v_cvt_pk_bf16_f32 v11, v11, v12
	v_lshl_add_u64 v[12:13], v[6:7], 0, v[2:3]
	global_store_dword v[12:13], v11, off
.LBB0_1526:
	s_or_b64 exec, exec, s[0:1]
	v_mul_f32_e32 v11, v64, v5
	s_waitcnt lgkmcnt(0)
	ds_bpermute_b32 v12, v10, v11
	s_and_saveexec_b64 s[0:1], s[2:3]
	s_cbranch_execz .LBB0_1528
	v_lshl_add_u64 v[14:15], v[8:9], 0, v[2:3]
	v_mov_b32_e32 v13, v245
	v_lshlrev_b32_e32 v14, 16, v13
	v_and_b32_e32 v13, 0xffff0000, v13
	v_mul_f32_e32 v11, v11, v14
	s_waitcnt lgkmcnt(0)
	v_mul_f32_e32 v12, v12, v13
	v_cvt_pk_bf16_f32 v11, v11, v12
	v_lshl_add_u64 v[12:13], v[6:7], 0, v[2:3]
	global_store_dword v[12:13], v11, off offset:64
.LBB0_1528:
	s_or_b64 exec, exec, s[0:1]
	v_mul_f32_e32 v11, v48, v5
	s_waitcnt lgkmcnt(0)
	ds_bpermute_b32 v12, v10, v11
	s_and_saveexec_b64 s[0:1], s[2:3]
	s_cbranch_execz .LBB0_1530
	v_lshl_add_u64 v[14:15], v[8:9], 0, v[2:3]
	v_mov_b32_e32 v13, v246
	v_lshlrev_b32_e32 v14, 16, v13
	v_and_b32_e32 v13, 0xffff0000, v13
	v_mul_f32_e32 v11, v11, v14
	s_waitcnt lgkmcnt(0)
	v_mul_f32_e32 v12, v12, v13
	v_cvt_pk_bf16_f32 v11, v11, v12
	v_lshl_add_u64 v[12:13], v[6:7], 0, v[2:3]
	global_store_dword v[12:13], v11, off offset:128
.LBB0_1530:
	s_or_b64 exec, exec, s[0:1]
	v_mul_f32_e32 v5, v32, v5
	ds_bpermute_b32 v11, v10, v5
	s_and_saveexec_b64 s[0:1], s[2:3]
	s_cbranch_execz .LBB0_1532
	v_lshl_add_u64 v[8:9], v[8:9], 0, v[2:3]
	v_lshl_add_u64 v[6:7], v[6:7], 0, v[2:3]
	v_mov_b32_e32 v8, v247
	v_lshlrev_b32_e32 v9, 16, v8
	v_and_b32_e32 v8, 0xffff0000, v8
	v_mul_f32_e32 v5, v5, v9
	s_waitcnt lgkmcnt(0)
	v_mul_f32_e32 v8, v11, v8
	v_cvt_pk_bf16_f32 v5, v5, v8
	global_store_dword v[6:7], v5, off offset:192

;     __device__ __forceinline__ bool next(int i, Unit& u) const { if (!order_tile(i, G, c, nM, nN, u.pm, u.pn)) return false; u.A = A0 + (size_t)u.pm * tstep; u.B = B0 + (size_t)u.pn * tstep; return true; }
;     __device__ __forceinline__ bool next(int i, Unit& u) const { if (!order_tile(i, G, c, nM, nN, u.pm, u.pn)) return false; u.A = A0 + (size_t)(u.pn >> 1) * groupA + (size_t)u.pm * tstep; u.B = B0 + (size_t)u.pn * tstep; return true; }
; #define PG8_STAGE(bufoff, gbase, voff) do { _Pragma("unroll") for (int _i = 0; _i < 2; ++_i) glds16_s((const void*)((const char*)(gbase) + _i * r64), (voff), ldsb + (unsigned)(bufoff) + ldsw + _i * 8192u); } while (0)
; #define PG8_WAIT_V(n) asm volatile("s_waitcnt vmcnt(" #n ")" ::: "memory")
; #define PG8_BAR __builtin_amdgcn_s_barrier()
; template <class Epi, class Sched, bool FP8 = false>
; __device__ __forceinline__ void gemm_phase(LAS unsigned char* lds, const int Kb, const int nt  , const Sched& S, const Epi& E) {
;     ...
;     { int R, C; stage_rc(tid * 16, R, C); const int Rb = Epi::PERM ? ((R & ~31) + perm32(R & 31)) : R;
;         voffA = (unsigned)(R * Kb + C * 2); voffB = (unsigned)(Rb * Kb + C * 2); }
;     const size_t r64 = (size_t)64 * Kb;
;     const size_t kstep = (size_t)(BK * 2);
;     const size_t hstep = (size_t)HALF * Kb;
;     const unsigned ldsw = (unsigned)wid * 1024u, ldsb = (unsigned)(uintptr_t)lds;
;     const int aoff = lds_byte(wr * 64 + fr, fq * 8), boff = lds_byte(wc * 32 + fr, fq * 8);
;     ...
;     Unit cur, nxt; int ui = 0;
;     if (!S.next(0, cur)) return;
;     f32x4 acc[2][2][4][2];
; #pragma unroll
;     for (int a = 0; a < 2; ++a)
; #pragma unroll
;         for (int b = 0; b < 2; ++b)
; #pragma unroll
;             for (int m = 0; m < 4; ++m)
; #pragma unroll
;                 for (int n = 0; n < 2; ++n) acc[a][b][m][n] = (f32x4){0.f, 0.f, 0.f, 0.f};
;     bf16x8 At[4][2], B0[2][2], B1[2][2]; i32x8 A8[4], B08[2], B18[2];
;     const char* cA = cur.A; const char* cB = cur.B;
;     PG8_STAGE(PG8_SB(0, 0), cB, voffB); PG8_STAGE(PG8_SA(0, 0), cA, voffA); PG8_STAGE(PG8_SB(0, 1), cB + hstep, voffB); PG8_STAGE(PG8_SA(0, 1), cA + hstep, voffA);
;     if (wr == 1) PG8_BAR;
;     PG8_WAIT_V(4); PG8_BAR;
;     PG8_STAGE(PG8_SB(1, 0), cB + kstep, voffB); PG8_STAGE(PG8_SA(1, 0), cA + kstep, voffA); PG8_STAGE(PG8_SB(1, 1), cB + hstep + kstep, voffB);
;     PG8_WAIT_V(6); PG8_BAR;
.LBB0_1706:
	v_readlane_b32 s4, v241, 5
	v_readlane_b32 s5, v241, 6
	s_add_u32 s4, s4, 0x56f00000
	s_addc_u32 s5, s5, 0
	s_lshl_b32 s3, s3, 5
	s_and_b32 s46, s3, 0x60
	s_lshl_b32 s45, s6, 6
	s_lshl_b32 s8, s6, 13
	s_lshl_b32 s3, s46, 7
	s_add_u32 s6, s24, 0x80
	s_addc_u32 s7, s25, 0
	s_add_i32 s47, s37, 0x18000
	s_waitcnt vmcnt(4)
	s_barrier
	s_mov_b32 s9, m0
	s_mov_b32 m0, s47
	s_nop 0
	global_load_lds_dwordx4 v1, s[6:7]
	s_mov_b32 m0, s9
	s_add_u32 s6, s24, 0x40080
	s_addc_u32 s7, s25, 0
	s_add_i32 s48, s37, 0x1a000
	s_mov_b32 s9, m0
	s_mov_b32 m0, s48
	s_nop 0
	global_load_lds_dwordx4 v1, s[6:7]
	s_mov_b32 m0, s9
	s_add_u32 s6, s22, 0x80
	s_addc_u32 s7, s23, 0
	s_add_i32 s49, s37, 0x8000
	s_mov_b32 s9, m0
	s_mov_b32 m0, s49
	s_nop 0
	global_load_lds_dwordx4 v1, s[6:7]
	s_mov_b32 m0, s9
	s_add_u32 s6, s22, 0x40080
	s_addc_u32 s7, s23, 0
	s_add_i32 s50, s37, 0xa000
	s_mov_b32 s9, m0
	s_mov_b32 m0, s50
	s_nop 0
	global_load_lds_dwordx4 v1, s[6:7]
	s_mov_b32 m0, s9
	s_add_u32 s6, s24, 0x80080
	s_addc_u32 s7, s25, 0
	s_add_i32 s51, s37, 0x1c000
	v_lshlrev_b32_e32 v3, 6, v0
	v_lshlrev_b32_e32 v4, 2, v0
	s_mov_b32 s9, m0
	s_mov_b32 m0, s51
	s_nop 0
	global_load_lds_dwordx4 v1, s[6:7]
	s_mov_b32 m0, s9
	s_add_u32 s6, s24, 0xc0080
	v_and_b32_e32 v2, 48, v0
	v_and_b32_e32 v3, 0x3c0, v3
	v_and_b32_e32 v4, 32, v4
	s_addc_u32 s7, s25, 0
	s_add_i32 s52, s37, 0x1e000
	s_mov_b32 s9, m0
	s_mov_b32 m0, s52
	s_nop 0
	global_load_lds_dwordx4 v1, s[6:7]
	s_mov_b32 m0, s9
	v_bitop3_b32 v2, v3, v4, v2 bitop3:0x36
	s_waitcnt vmcnt(6)
	s_add_i32 s3, s3, 0
	s_add_i32 s53, s37, 0xc000
	s_add_i32 s54, s37, 0xe000
	v_add_u32_e32 v3, s3, v2
	v_add_u32_e32 v2, 0, v2
	s_cmp_lg_u64 s[76:77], 0
	s_waitcnt vmcnt(5)
	v_add_u32_e32 v138, 0x10000, v3
	v_add_u32_e32 v139, 0x10400, v3
	v_add_u32_e32 v140, 0x10800, v3
	v_add_u32_e32 v141, 0x10c00, v3
	s_waitcnt vmcnt(4)
	v_add_u32_e32 v142, 0x14000, v3
	v_add_u32_e32 v143, 0x14400, v3
	v_add_u32_e32 v144, 0x14800, v3
	v_add_u32_e32 v145, 0x14c00, v3
	s_waitcnt vmcnt(0)
	v_add_u32_e32 v146, 0x18000, v3
	v_add_u32_e32 v147, 0x18400, v3
	v_add_u32_e32 v148, 0x18800, v3
	v_add_u32_e32 v149, 0x18c00, v3
	v_add_u32_e32 v150, 0x1c000, v3
	v_add_u32_e32 v151, 0x1c400, v3
	v_add_u32_e32 v152, 0x1c800, v3
	v_add_u32_e32 v153, 0x1cc00, v3
	s_cselect_b64 s[6:7], -1, 0
	v_add_u32_e32 v154, s8, v2
	s_mov_b64 s[8:9], 0x48000
	s_mov_b64 s[10:11], 0x50000
	s_mov_b64 s[12:13], 0x58000
	s_mov_b64 s[18:19], s[22:23]
	s_mov_b64 s[20:21], s[24:25]
	s_barrier
	s_branch .LBB0_1708
	s_nop 0
	s_nop 0
	s_nop 0
	s_nop 0
	s_nop 0
	s_nop 0
